# attention: tile+2 LDS-DMA issue block moved from the tile top to behind the K-fragment ds_reads (runs in the LDS latency shadow)
# baseline (speedup 1.0000x reference)
; #define LAS __attribute__((address_space(3)))
; __device__ __forceinline__ int crow(int r, int hi) { return (r & 3) + 8 * (r >> 2) + 4 * hi; }
; #define AT_LOAD(j) do { _Pragma("unroll") for (int i = 0; i < 2; ++i) { const int id = tid + 512 * i, row = id >> 4, c16 = id & 15; \
;         rk[i] = *(const u32x4*)(kbase + (size_t)(64 * (j) + row) * PW + c16 * 8); rv[i] = *(const u32x4*)(vbase + (size_t)(64 * (j) + row) * PW + c16 * 8); } } while (0)
; __device__ __forceinline__ void attn_unit(const Frame& F, const bf16* __restrict__ proj, bf16* mix, const float* relb, const float* subg, int h, int qb, float lam, float one_m_li) {
;     ...
;     for (int j = 0; j < NT; ++j) {
;         const int cur = j & 1;
;         bf16x8 kf[2][2];
;         const LAS unsigned char* Kb = lds + cur * STAGE + m * 8192;
;         if (j <= cw) {
; #pragma unroll
;             for (int d0 = 0; d0 < 2; ++d0) { const int c = 2 * d0 + hi; kf[d0][0] = *(const LAS bf16x8*)(Kb + c * 1024 + ((r32 ^ c) * 16)); kf[d0][1] = *(const LAS bf16x8*)(Kb + c * 1024 + ((r32 ^ c) * 16) + 512); } }
;         __builtin_amdgcn_sched_barrier(0);
;         if (j + 1 < NT) AT_STORE(cur ^ 1);
;         if (j + 2 < NT) AT_LOAD(j + 2);
;         if (j <= cw) {
;             f32x16 p0, p1;
; #pragma unroll
;             for (int d0 = 0; d0 < 4; ++d0) { const int c = 2 * d0 + hi;
;                 const bf16x8 a0 = (d0 < 2) ? kf[d0 & 1][0] : *(const LAS bf16x8*)(Kb + c * 1024 + ((r32 ^ c) * 16));
;                 const bf16x8 a1 = (d0 < 2) ? kf[d0 & 1][1] : *(const LAS bf16x8*)(Kb + c * 1024 + ((r32 ^ c) * 16) + 512);
;                 if (d0 == 0) { p0 = __builtin_amdgcn_mfma_f32_32x32x16_bf16(a0, qr[0], negm, 0, 0, 0); p1 = __builtin_amdgcn_mfma_f32_32x32x16_bf16(a1, qr[0], negm, 0, 0, 0); }
;                 else { p0 = __builtin_amdgcn_mfma_f32_32x32x16_bf16(a0, qr[d0], p0, 0, 0, 0); p1 = __builtin_amdgcn_mfma_f32_32x32x16_bf16(a1, qr[d0], p1, 0, 0, 0); } }
;             if (j >= cw - 2) {
;                 const int base = 64 * j - qrow + 192;
; #pragma unroll
;                 for (int r = 0; r < 16; ++r) { const int kv = crow(r, hi); p0[r] += lut[base + kv]; p1[r] += lut[base + kv + 32]; }
.LBB0_581:
	s_mov_b32 s88, s73
	s_add_i32 s79, s88, 0
	s_add_i32 s86, s13, -1
	s_add_i32 s87, s79, s40
	s_cmp_gt_u32 s86, s10
	s_cbranch_scc1 .Ldma_idle
	v_add3_u32 v81, s79, v209, v210
	v_add3_u32 v80, s79, v211, v212
	v_add3_u32 v172, s79, v214, v215
	v_add3_u32 v173, s79, v216, v217
	ds_read_b128 v[144:147], v81
	ds_read_b128 v[148:151], v81 offset:8192
	ds_read_b128 v[152:155], v80
	ds_read_b128 v[156:159], v80 offset:8192
	ds_read_b128 v[168:171], v172
	ds_read_b128 v[176:179], v172 offset:8192
	ds_read_b128 v[180:183], v173
	ds_read_b128 v[196:199], v173 offset:8192
	s_cmp_ge_u32 s86, s12
	s_cbranch_scc1 .Ldma_skip
	s_sub_i32 s101, s88, 0x8000
	s_cmp_eq_u32 s88, 0
	s_cselect_b32 s101, 0x10000, s101
	s_add_i32 s101, s101, s100
	s_mov_b32 m0, s101
	s_nop 0
	global_load_lds_dwordx4 v128, s[50:51]
	s_add_i32 m0, s101, 0x400
	s_nop 0
	global_load_lds_dwordx4 v129, s[50:51]
	s_add_i32 m0, s101, 0x4000
	s_nop 0
	global_load_lds_dwordx4 v130, s[50:51]
	s_add_i32 m0, s101, 0x4400
	s_nop 0
	global_load_lds_dwordx4 v131, s[50:51]
	s_add_u32 s50, s50, 0x90000
	s_addc_u32 s51, s51, 0
.Ldma_skip:
	s_waitcnt lgkmcnt(7)
	v_mfma_f32_32x32x16_bf16 v[96:111], v[144:147], v[112:115], v[64:79]
	s_waitcnt lgkmcnt(6)
	v_mfma_f32_32x32x16_bf16 v[80:95], v[148:151], v[112:115], v[64:79]
	s_waitcnt lgkmcnt(5)
	v_mfma_f32_32x32x16_bf16 v[96:111], v[152:155], v[116:119], v[96:111]
	s_waitcnt lgkmcnt(4)
	v_mfma_f32_32x32x16_bf16 v[80:95], v[156:159], v[116:119], v[80:95]
	s_waitcnt lgkmcnt(3)
	v_mfma_f32_32x32x16_bf16 v[96:111], v[168:171], v[120:123], v[96:111]
	s_waitcnt lgkmcnt(2)
	v_mfma_f32_32x32x16_bf16 v[80:95], v[176:179], v[120:123], v[80:95]
	s_waitcnt lgkmcnt(1)
	v_mfma_f32_32x32x16_bf16 v[96:111], v[180:183], v[124:127], v[96:111]
	s_waitcnt lgkmcnt(0)
	v_mfma_f32_32x32x16_bf16 v[80:95], v[196:199], v[124:127], v[80:95]
	s_cmp_lt_i32 s86, s11
	s_cbranch_scc1 .LBB0_590
	v_add_u32_e32 v223, s60, v222
	v_add_u32_e32 v168, 0x18500, v223
	v_add_u32_e32 v170, 0x18580, v223
	ds_read2_b32 v[168:169], v168 offset1:1
	ds_read2_b32 v[170:171], v170 offset1:1
	v_add_u32_e32 v172, 0x18508, v223
	v_add_u32_e32 v174, 0x18588, v223
	v_add_u32_e32 v176, 0x18520, v223
	v_add_u32_e32 v178, 0x185a0, v223
	v_add_u32_e32 v180, 0x18528, v223
	v_add_u32_e32 v182, 0x185a8, v223
	v_add_u32_e32 v184, 0x18540, v223
	v_add_u32_e32 v196, 0x185c0, v223
	v_add_u32_e32 v198, 0x18548, v223
	v_add_u32_e32 v200, 0x185c8, v223
	v_add_u32_e32 v202, 0x18560, v223
	v_add_u32_e32 v224, 0x185e0, v223
	v_add_u32_e32 v226, 0x18568, v223
	v_add_u32_e32 v223, 0x185e8, v223
	ds_read2_b32 v[172:173], v172 offset1:1
	ds_read2_b32 v[174:175], v174 offset1:1
	ds_read2_b32 v[176:177], v176 offset1:1
	ds_read2_b32 v[178:179], v178 offset1:1
	ds_read2_b32 v[180:181], v180 offset1:1
	ds_read2_b32 v[182:183], v182 offset1:1
	ds_read2_b32 v[184:185], v184 offset1:1
	ds_read2_b32 v[196:197], v196 offset1:1
	ds_read2_b32 v[198:199], v198 offset1:1
	ds_read2_b32 v[200:201], v200 offset1:1
	ds_read2_b32 v[202:203], v202 offset1:1
	ds_read2_b32 v[224:225], v224 offset1:1
	ds_read2_b32 v[226:227], v226 offset1:1
	s_waitcnt lgkmcnt(14)
	v_pk_add_f32 v[96:97], v[96:97], v[168:169]
	ds_read2_b32 v[168:169], v223 offset1:1
	s_waitcnt lgkmcnt(3)
	v_pk_add_f32 v[108:109], v[108:109], v[202:203]
	v_pk_add_f32 v[106:107], v[106:107], v[198:199]
	s_waitcnt lgkmcnt(1)
	v_pk_add_f32 v[110:111], v[110:111], v[226:227]
	v_pk_add_f32 v[104:105], v[104:105], v[184:185]
	v_pk_add_f32 v[102:103], v[102:103], v[180:181]
	v_pk_add_f32 v[100:101], v[100:101], v[176:177]
	v_pk_add_f32 v[98:99], v[98:99], v[172:173]
	s_waitcnt lgkmcnt(0)
	v_pk_add_f32 v[94:95], v[94:95], v[168:169]
	v_pk_add_f32 v[92:93], v[92:93], v[224:225]
	v_pk_add_f32 v[90:91], v[90:91], v[200:201]
	v_pk_add_f32 v[88:89], v[88:89], v[196:197]
	v_pk_add_f32 v[86:87], v[86:87], v[182:183]
	v_pk_add_f32 v[84:85], v[84:85], v[178:179]
	v_pk_add_f32 v[82:83], v[82:83], v[174:175]
	v_pk_add_f32 v[80:81], v[80:81], v[170:171]

; #define AT_LOAD(j) do { _Pragma("unroll") for (int i = 0; i < 2; ++i) { const int id = tid + 512 * i, row = id >> 4, c16 = id & 15; \
;         rk[i] = *(const u32x4*)(kbase + (size_t)(64 * (j) + row) * PW + c16 * 8); rv[i] = *(const u32x4*)(vbase + (size_t)(64 * (j) + row) * PW + c16 * 8); } } while (0)
; #define AT_STORE(buf) do { _Pragma("unroll") for (int i = 0; i < 2; ++i) { const int id = tid + 512 * i, row = id >> 4, c16 = id & 15, mk = c16 >> 3, c = c16 & 7; \
;         *(LAS u32x4*)(lds + (buf) * STAGE + mk * 8192 + c * 1024 + ((row ^ c) * 16)) = rk[i]; \
;         *(LAS u32x4*)(lds + (buf) * STAGE + 16384 + (c16 >> 2) * 4096 + row * 64 + (c16 & 3) * 16) = rv[i]; } } while (0)
; __device__ __forceinline__ void attn_unit(const Frame& F, const bf16* __restrict__ proj, bf16* mix, const float* relb, const float* subg, int h, int qb, float lam, float one_m_li) {
;     ...
;         if (j + 1 < NT) AT_STORE(cur ^ 1);
;         if (j + 2 < NT) AT_LOAD(j + 2);
.Ldma_idle:
	s_cmp_ge_u32 s86, s12
	s_cbranch_scc1 .LBB0_580
	s_sub_i32 s101, s88, 0x8000
	s_cmp_eq_u32 s88, 0
	s_cselect_b32 s101, 0x10000, s101
	s_add_i32 s101, s101, s100
	s_mov_b32 m0, s101
	s_nop 0
	global_load_lds_dwordx4 v128, s[50:51]
	s_add_i32 m0, s101, 0x400
	s_nop 0
	global_load_lds_dwordx4 v129, s[50:51]
	s_add_i32 m0, s101, 0x4000
	s_nop 0
	global_load_lds_dwordx4 v130, s[50:51]
	s_add_i32 m0, s101, 0x4400
	s_nop 0
	global_load_lds_dwordx4 v131, s[50:51]
	s_add_u32 s50, s50, 0x90000
	s_addc_u32 s51, s51, 0
	s_branch .LBB0_580
